# k-snake visiting accumulators weight-fragment-stationary (B shared at six of seven pair boundaries) in 4 GEMM loops, same stack as v100
# speedup vs baseline: 1.0069x; 1.0055x over previous
.LBB0_114:
	ds_read_b128 v[130:133], v220
	ds_read_b128 v[134:137], v220 offset:1024
	ds_read_b128 v[138:141], v220 offset:2048
	ds_read_b128 v[142:145], v220 offset:3072
	ds_read_b128 v[146:149], v221
	ds_read_b128 v[150:153], v221 offset:1024
	ds_read_b128 v[154:157], v221 offset:2048
	ds_read_b128 v[158:161], v221 offset:3072
	s_add_i32 s46, s64, 0xfff80080
	s_cmp_eq_u32 s84, 28
	s_cselect_b32 s87, s62, s46
	s_cselect_b32 s86, s63, s65
	s_or_b32 s85, s87, 0x80
	s_mov_b32 m0, s93
	ds_read_b128 v[162:165], v222
	ds_read_b128 v[166:169], v222 offset:1024
	ds_read_b128 v[170:173], v222 offset:2048
	ds_read_b128 v[174:177], v222 offset:3072
	ds_read_b128 v[178:181], v222 offset:4096
	ds_read_b128 v[182:185], v222 offset:5120
	ds_read_b128 v[186:189], v222 offset:6144
	ds_read_b128 v[212:215], v222 offset:7168
	buffer_load_dwordx4 v1, s[40:43], s64 offen lds
	s_mov_b32 m0, s94
	s_nop 0
	buffer_load_dwordx4 v216, s[40:43], s64 offen lds
	s_waitcnt vmcnt(8)
	s_waitcnt lgkmcnt(0)
	s_barrier
	s_waitcnt lgkmcnt(7)
	v_mfma_f32_16x16x32_bf16 v[126:129], v[130:133], v[162:165], v[126:129]
	v_mfma_f32_16x16x32_bf16 v[126:129], v[134:137], v[166:169], v[126:129]
	s_waitcnt lgkmcnt(5)
	v_mfma_f32_16x16x32_bf16 v[114:117], v[134:137], v[174:177], v[114:117]
	v_mfma_f32_16x16x32_bf16 v[114:117], v[130:133], v[170:173], v[114:117]
	s_waitcnt lgkmcnt(3)
	v_mfma_f32_16x16x32_bf16 v[102:105], v[130:133], v[178:181], v[102:105]
	v_mfma_f32_16x16x32_bf16 v[102:105], v[134:137], v[182:185], v[102:105]
	s_waitcnt lgkmcnt(1)
	v_mfma_f32_16x16x32_bf16 v[86:89], v[134:137], v[212:215], v[86:89]
	v_mfma_f32_16x16x32_bf16 v[86:89], v[130:133], v[186:189], v[86:89]
	v_mfma_f32_16x16x32_bf16 v[78:81], v[138:141], v[186:189], v[78:81]
	v_mfma_f32_16x16x32_bf16 v[78:81], v[142:145], v[212:215], v[78:81]
	v_mfma_f32_16x16x32_bf16 v[94:97], v[142:145], v[182:185], v[94:97]
	v_mfma_f32_16x16x32_bf16 v[94:97], v[138:141], v[178:181], v[94:97]
	v_mfma_f32_16x16x32_bf16 v[106:109], v[138:141], v[170:173], v[106:109]
	v_mfma_f32_16x16x32_bf16 v[106:109], v[142:145], v[174:177], v[106:109]
	s_waitcnt lgkmcnt(0)
	v_mfma_f32_16x16x32_bf16 v[122:125], v[142:145], v[166:169], v[122:125]
	v_mfma_f32_16x16x32_bf16 v[122:125], v[138:141], v[162:165], v[122:125]
	v_mfma_f32_16x16x32_bf16 v[118:121], v[146:149], v[162:165], v[118:121]
	v_mfma_f32_16x16x32_bf16 v[118:121], v[150:153], v[166:169], v[118:121]
	v_mfma_f32_16x16x32_bf16 v[98:101], v[150:153], v[174:177], v[98:101]
	v_mfma_f32_16x16x32_bf16 v[98:101], v[146:149], v[170:173], v[98:101]
	v_mfma_f32_16x16x32_bf16 v[82:85], v[146:149], v[178:181], v[82:85]
	v_mfma_f32_16x16x32_bf16 v[82:85], v[150:153], v[182:185], v[82:85]
	v_mfma_f32_16x16x32_bf16 v[70:73], v[150:153], v[212:215], v[70:73]
	v_mfma_f32_16x16x32_bf16 v[70:73], v[146:149], v[186:189], v[70:73]
	v_mfma_f32_16x16x32_bf16 v[66:69], v[154:157], v[186:189], v[66:69]
	v_mfma_f32_16x16x32_bf16 v[66:69], v[158:161], v[212:215], v[66:69]
	v_mfma_f32_16x16x32_bf16 v[74:77], v[158:161], v[182:185], v[74:77]
	v_mfma_f32_16x16x32_bf16 v[74:77], v[154:157], v[178:181], v[74:77]
	v_mfma_f32_16x16x32_bf16 v[90:93], v[154:157], v[170:173], v[90:93]
	v_mfma_f32_16x16x32_bf16 v[90:93], v[158:161], v[174:177], v[90:93]
	v_mfma_f32_16x16x32_bf16 v[110:113], v[158:161], v[166:169], v[110:113]
	v_mfma_f32_16x16x32_bf16 v[110:113], v[154:157], v[162:165], v[110:113]
	s_barrier
	s_mov_b32 m0, s69
	s_mov_b32 s46, s42
	s_mov_b32 s47, s43
	ds_read_b128 v[162:165], v222 offset:16384
	ds_read_b128 v[166:169], v222 offset:17408
	ds_read_b128 v[170:173], v222 offset:18432
	ds_read_b128 v[174:177], v222 offset:19456
	ds_read_b128 v[178:181], v222 offset:20480
	ds_read_b128 v[182:185], v222 offset:21504
	ds_read_b128 v[186:189], v222 offset:22528
	ds_read_b128 v[212:215], v222 offset:23552
	buffer_load_dwordx4 v191, s[44:47], s86 offen lds
	s_mov_b32 m0, s70
	s_add_i32 s88, s86, 0x80000
	buffer_load_dwordx4 v217, s[44:47], s86 offen lds
	s_mov_b32 m0, s71
	s_nop 0
	buffer_load_dwordx4 v191, s[44:47], s88 offen lds
	s_mov_b32 m0, s72
	s_nop 0
	buffer_load_dwordx4 v217, s[44:47], s88 offen lds
	s_mov_b32 m0, s68
	s_nop 0
	buffer_load_dwordx4 v1, s[40:43], s87 offen lds
	s_mov_b32 m0, s73
	s_nop 0
	buffer_load_dwordx4 v216, s[40:43], s87 offen lds
	s_waitcnt vmcnt(8)
	s_waitcnt lgkmcnt(0)
	s_barrier
	s_waitcnt lgkmcnt(7)
	v_mfma_f32_16x16x32_bf16 v[62:65], v[130:133], v[162:165], v[62:65]
	v_mfma_f32_16x16x32_bf16 v[62:65], v[134:137], v[166:169], v[62:65]
	s_waitcnt lgkmcnt(5)
	v_mfma_f32_16x16x32_bf16 v[54:57], v[134:137], v[174:177], v[54:57]
	v_mfma_f32_16x16x32_bf16 v[54:57], v[130:133], v[170:173], v[54:57]
	s_waitcnt lgkmcnt(3)
	v_mfma_f32_16x16x32_bf16 v[38:41], v[130:133], v[178:181], v[38:41]
	v_mfma_f32_16x16x32_bf16 v[38:41], v[134:137], v[182:185], v[38:41]
	s_waitcnt lgkmcnt(1)
	v_mfma_f32_16x16x32_bf16 v[22:25], v[134:137], v[212:215], v[22:25]
	v_mfma_f32_16x16x32_bf16 v[22:25], v[130:133], v[186:189], v[22:25]
	v_mfma_f32_16x16x32_bf16 v[14:17], v[138:141], v[186:189], v[14:17]
	v_mfma_f32_16x16x32_bf16 v[14:17], v[142:145], v[212:215], v[14:17]
	v_mfma_f32_16x16x32_bf16 v[30:33], v[142:145], v[182:185], v[30:33]
	v_mfma_f32_16x16x32_bf16 v[30:33], v[138:141], v[178:181], v[30:33]
	v_mfma_f32_16x16x32_bf16 v[46:49], v[138:141], v[170:173], v[46:49]
	v_mfma_f32_16x16x32_bf16 v[46:49], v[142:145], v[174:177], v[46:49]
	s_waitcnt lgkmcnt(0)
	v_mfma_f32_16x16x32_bf16 v[58:61], v[142:145], v[166:169], v[58:61]
	v_mfma_f32_16x16x32_bf16 v[58:61], v[138:141], v[162:165], v[58:61]
	v_mfma_f32_16x16x32_bf16 v[50:53], v[146:149], v[162:165], v[50:53]
	v_mfma_f32_16x16x32_bf16 v[50:53], v[150:153], v[166:169], v[50:53]
	v_mfma_f32_16x16x32_bf16 v[34:37], v[150:153], v[174:177], v[34:37]
	v_mfma_f32_16x16x32_bf16 v[34:37], v[146:149], v[170:173], v[34:37]
	v_mfma_f32_16x16x32_bf16 v[18:21], v[146:149], v[178:181], v[18:21]
	v_mfma_f32_16x16x32_bf16 v[18:21], v[150:153], v[182:185], v[18:21]
	v_mfma_f32_16x16x32_bf16 v[6:9], v[150:153], v[212:215], v[6:9]
	v_mfma_f32_16x16x32_bf16 v[6:9], v[146:149], v[186:189], v[6:9]
	v_mfma_f32_16x16x32_bf16 v[2:5], v[154:157], v[186:189], v[2:5]
	v_mfma_f32_16x16x32_bf16 v[2:5], v[158:161], v[212:215], v[2:5]
	v_mfma_f32_16x16x32_bf16 v[10:13], v[158:161], v[182:185], v[10:13]
	v_mfma_f32_16x16x32_bf16 v[10:13], v[154:157], v[178:181], v[10:13]
	v_mfma_f32_16x16x32_bf16 v[26:29], v[154:157], v[170:173], v[26:29]
	v_mfma_f32_16x16x32_bf16 v[26:29], v[158:161], v[174:177], v[26:29]
	v_mfma_f32_16x16x32_bf16 v[42:45], v[158:161], v[166:169], v[42:45]
	v_mfma_f32_16x16x32_bf16 v[42:45], v[154:157], v[162:165], v[42:45]
	s_barrier
	ds_read_b128 v[130:133], v223
	ds_read_b128 v[134:137], v223 offset:1024
	ds_read_b128 v[138:141], v223 offset:2048
	ds_read_b128 v[142:145], v223 offset:3072
	ds_read_b128 v[146:149], v224
	ds_read_b128 v[150:153], v224 offset:1024
	ds_read_b128 v[154:157], v224 offset:2048
	ds_read_b128 v[158:161], v224 offset:3072
	s_add_i32 s87, s87, 0x80000
	s_mov_b32 m0, s74
	ds_read_b128 v[162:165], v222 offset:32768
	ds_read_b128 v[166:169], v222 offset:33792
	ds_read_b128 v[170:173], v222 offset:34816
	ds_read_b128 v[174:177], v222 offset:35840
	ds_read_b128 v[178:181], v222 offset:36864
	ds_read_b128 v[182:185], v222 offset:37888
	ds_read_b128 v[186:189], v222 offset:38912
	ds_read_b128 v[212:215], v222 offset:39936
	buffer_load_dwordx4 v1, s[40:43], s87 offen lds
	s_mov_b32 m0, s75
	s_nop 0
	buffer_load_dwordx4 v216, s[40:43], s87 offen lds
	s_waitcnt vmcnt(8)
	s_waitcnt lgkmcnt(0)
	s_barrier
	s_waitcnt lgkmcnt(7)
	v_mfma_f32_16x16x32_bf16 v[126:129], v[130:133], v[162:165], v[126:129]
	v_mfma_f32_16x16x32_bf16 v[126:129], v[134:137], v[166:169], v[126:129]
	s_waitcnt lgkmcnt(5)
	v_mfma_f32_16x16x32_bf16 v[114:117], v[134:137], v[174:177], v[114:117]
	v_mfma_f32_16x16x32_bf16 v[114:117], v[130:133], v[170:173], v[114:117]
	s_waitcnt lgkmcnt(3)
	v_mfma_f32_16x16x32_bf16 v[102:105], v[130:133], v[178:181], v[102:105]
	v_mfma_f32_16x16x32_bf16 v[102:105], v[134:137], v[182:185], v[102:105]
	s_waitcnt lgkmcnt(1)
	v_mfma_f32_16x16x32_bf16 v[86:89], v[134:137], v[212:215], v[86:89]
	v_mfma_f32_16x16x32_bf16 v[86:89], v[130:133], v[186:189], v[86:89]
	v_mfma_f32_16x16x32_bf16 v[78:81], v[138:141], v[186:189], v[78:81]
	v_mfma_f32_16x16x32_bf16 v[78:81], v[142:145], v[212:215], v[78:81]
	v_mfma_f32_16x16x32_bf16 v[94:97], v[142:145], v[182:185], v[94:97]
	v_mfma_f32_16x16x32_bf16 v[94:97], v[138:141], v[178:181], v[94:97]
	v_mfma_f32_16x16x32_bf16 v[106:109], v[138:141], v[170:173], v[106:109]
	v_mfma_f32_16x16x32_bf16 v[106:109], v[142:145], v[174:177], v[106:109]
	s_waitcnt lgkmcnt(0)
	v_mfma_f32_16x16x32_bf16 v[122:125], v[142:145], v[166:169], v[122:125]
	v_mfma_f32_16x16x32_bf16 v[122:125], v[138:141], v[162:165], v[122:125]
	v_mfma_f32_16x16x32_bf16 v[118:121], v[146:149], v[162:165], v[118:121]
	v_mfma_f32_16x16x32_bf16 v[118:121], v[150:153], v[166:169], v[118:121]
	v_mfma_f32_16x16x32_bf16 v[98:101], v[150:153], v[174:177], v[98:101]
	v_mfma_f32_16x16x32_bf16 v[98:101], v[146:149], v[170:173], v[98:101]
	v_mfma_f32_16x16x32_bf16 v[82:85], v[146:149], v[178:181], v[82:85]
	v_mfma_f32_16x16x32_bf16 v[82:85], v[150:153], v[182:185], v[82:85]
	v_mfma_f32_16x16x32_bf16 v[70:73], v[150:153], v[212:215], v[70:73]
	v_mfma_f32_16x16x32_bf16 v[70:73], v[146:149], v[186:189], v[70:73]
	v_mfma_f32_16x16x32_bf16 v[66:69], v[154:157], v[186:189], v[66:69]
	v_mfma_f32_16x16x32_bf16 v[66:69], v[158:161], v[212:215], v[66:69]
	v_mfma_f32_16x16x32_bf16 v[74:77], v[158:161], v[182:185], v[74:77]
	v_mfma_f32_16x16x32_bf16 v[74:77], v[154:157], v[178:181], v[74:77]
	v_mfma_f32_16x16x32_bf16 v[90:93], v[154:157], v[170:173], v[90:93]
	v_mfma_f32_16x16x32_bf16 v[90:93], v[158:161], v[174:177], v[90:93]
	v_mfma_f32_16x16x32_bf16 v[110:113], v[158:161], v[166:169], v[110:113]
	v_mfma_f32_16x16x32_bf16 v[110:113], v[154:157], v[162:165], v[110:113]
	s_barrier
	s_mov_b32 m0, s79
	s_or_b32 s87, s86, 0x80
	ds_read_b128 v[162:165], v222 offset:49152
	ds_read_b128 v[166:169], v222 offset:50176
	ds_read_b128 v[170:173], v222 offset:51200
	ds_read_b128 v[174:177], v222 offset:52224
	ds_read_b128 v[178:181], v222 offset:53248
	ds_read_b128 v[182:185], v222 offset:54272
	ds_read_b128 v[186:189], v222 offset:55296
	ds_read_b128 v[212:215], v222 offset:56320
	buffer_load_dwordx4 v191, s[44:47], s87 offen lds
	s_mov_b32 m0, s80
	s_add_i32 s86, s86, 0x80080
	buffer_load_dwordx4 v217, s[44:47], s87 offen lds
	s_mov_b32 m0, s83
	s_nop 0
	buffer_load_dwordx4 v191, s[44:47], s86 offen lds
	s_mov_b32 m0, s92
	s_nop 0
	buffer_load_dwordx4 v217, s[44:47], s86 offen lds
	s_mov_b32 m0, s81
	s_nop 0
	buffer_load_dwordx4 v1, s[40:43], s85 offen lds
	s_mov_b32 m0, s82
	s_nop 0
	buffer_load_dwordx4 v216, s[40:43], s85 offen lds
	s_waitcnt vmcnt(8)
	s_waitcnt lgkmcnt(0)
	s_barrier
	s_waitcnt lgkmcnt(7)
	v_mfma_f32_16x16x32_bf16 v[62:65], v[130:133], v[162:165], v[62:65]
	v_mfma_f32_16x16x32_bf16 v[62:65], v[134:137], v[166:169], v[62:65]
	s_waitcnt lgkmcnt(5)
	v_mfma_f32_16x16x32_bf16 v[54:57], v[134:137], v[174:177], v[54:57]
	v_mfma_f32_16x16x32_bf16 v[54:57], v[130:133], v[170:173], v[54:57]
	s_waitcnt lgkmcnt(3)
	v_mfma_f32_16x16x32_bf16 v[38:41], v[130:133], v[178:181], v[38:41]
	v_mfma_f32_16x16x32_bf16 v[38:41], v[134:137], v[182:185], v[38:41]
	s_waitcnt lgkmcnt(1)
	v_mfma_f32_16x16x32_bf16 v[22:25], v[134:137], v[212:215], v[22:25]
	v_mfma_f32_16x16x32_bf16 v[22:25], v[130:133], v[186:189], v[22:25]
	v_mfma_f32_16x16x32_bf16 v[14:17], v[138:141], v[186:189], v[14:17]
	v_mfma_f32_16x16x32_bf16 v[14:17], v[142:145], v[212:215], v[14:17]
	v_mfma_f32_16x16x32_bf16 v[30:33], v[142:145], v[182:185], v[30:33]
	v_mfma_f32_16x16x32_bf16 v[30:33], v[138:141], v[178:181], v[30:33]
	v_mfma_f32_16x16x32_bf16 v[46:49], v[138:141], v[170:173], v[46:49]
	v_mfma_f32_16x16x32_bf16 v[46:49], v[142:145], v[174:177], v[46:49]
	s_waitcnt lgkmcnt(0)
	v_mfma_f32_16x16x32_bf16 v[58:61], v[142:145], v[166:169], v[58:61]
	v_mfma_f32_16x16x32_bf16 v[58:61], v[138:141], v[162:165], v[58:61]
	v_mfma_f32_16x16x32_bf16 v[50:53], v[146:149], v[162:165], v[50:53]
	v_mfma_f32_16x16x32_bf16 v[50:53], v[150:153], v[166:169], v[50:53]
	v_mfma_f32_16x16x32_bf16 v[34:37], v[150:153], v[174:177], v[34:37]
	v_mfma_f32_16x16x32_bf16 v[34:37], v[146:149], v[170:173], v[34:37]
	v_mfma_f32_16x16x32_bf16 v[18:21], v[146:149], v[178:181], v[18:21]
	v_mfma_f32_16x16x32_bf16 v[18:21], v[150:153], v[182:185], v[18:21]
	v_mfma_f32_16x16x32_bf16 v[6:9], v[150:153], v[212:215], v[6:9]
	v_mfma_f32_16x16x32_bf16 v[6:9], v[146:149], v[186:189], v[6:9]
	v_mfma_f32_16x16x32_bf16 v[2:5], v[154:157], v[186:189], v[2:5]
	v_mfma_f32_16x16x32_bf16 v[2:5], v[158:161], v[212:215], v[2:5]
	v_mfma_f32_16x16x32_bf16 v[10:13], v[158:161], v[182:185], v[10:13]
	v_mfma_f32_16x16x32_bf16 v[10:13], v[154:157], v[178:181], v[10:13]
	v_mfma_f32_16x16x32_bf16 v[26:29], v[154:157], v[170:173], v[26:29]
	v_mfma_f32_16x16x32_bf16 v[26:29], v[158:161], v[174:177], v[26:29]
	v_mfma_f32_16x16x32_bf16 v[42:45], v[158:161], v[166:169], v[42:45]
	v_mfma_f32_16x16x32_bf16 v[42:45], v[154:157], v[162:165], v[42:45]
	s_barrier
	s_add_i32 s84, s84, 2
	s_addk_i32 s64, 0x100
	s_addk_i32 s65, 0x100
	s_cmp_gt_u32 s84, 29
	s_cbranch_scc0 .LBB0_114
	s_and_b64 vcc, exec, s[56:57]
	s_cbranch_vccz .LBB0_127
	s_barrier
	s_cmp_gt_i32 s61, 23
	s_mov_b64 s[46:47], -1
	s_cbranch_scc1 .LBB0_128

.LBB0_686:
	v_add_u32_e32 v152, 0x10000, v138
	v_add_u32_e32 v168, 0x14000, v138
	ds_read_b128 v[140:143], v152
	ds_read_b128 v[144:147], v152 offset:1024
	ds_read_b128 v[148:151], v152 offset:2048
	ds_read_b128 v[152:155], v152 offset:3072
	ds_read_b128 v[156:159], v168
	ds_read_b128 v[160:163], v168 offset:1024
	ds_read_b128 v[164:167], v168 offset:2048
	ds_read_b128 v[168:171], v168 offset:3072
	s_add_i32 s10, s33, s52
	s_add_i32 s53, s27, s52
	s_add_i32 s11, s10, 0x1000
	s_addk_i32 s53, 0x1000
	s_cmp_eq_u32 s52, 0
	s_cselect_b32 s55, s49, s11
	s_cselect_b32 s54, s50, s53
	s_or_b32 s53, s55, 0x80
	s_add_i32 s10, s10, 0x80f80
	s_mov_b32 m0, s43
	ds_read_b128 v[172:175], v139
	ds_read_b128 v[176:179], v139 offset:1024
	ds_read_b128 v[180:183], v139 offset:2048
	ds_read_b128 v[184:187], v139 offset:3072
	ds_read_b128 v[188:191], v139 offset:4096
	ds_read_b128 v[192:195], v139 offset:5120
	ds_read_b128 v[196:199], v139 offset:6144
	ds_read_b128 v[200:203], v139 offset:7168
	buffer_load_dwordx4 v134, s[4:7], s10 offen lds
	s_mov_b32 m0, s44
	s_nop 0
	buffer_load_dwordx4 v136, s[4:7], s10 offen lds
	s_waitcnt vmcnt(8)
	s_waitcnt lgkmcnt(0)
	s_barrier
	s_waitcnt lgkmcnt(7)
	v_mfma_f32_16x16x32_bf16 v[126:129], v[140:143], v[172:175], v[126:129]
	v_mfma_f32_16x16x32_bf16 v[126:129], v[144:147], v[176:179], v[126:129]
	s_waitcnt lgkmcnt(5)
	v_mfma_f32_16x16x32_bf16 v[110:113], v[144:147], v[184:187], v[110:113]
	v_mfma_f32_16x16x32_bf16 v[110:113], v[140:143], v[180:183], v[110:113]
	s_waitcnt lgkmcnt(3)
	v_mfma_f32_16x16x32_bf16 v[98:101], v[140:143], v[188:191], v[98:101]
	v_mfma_f32_16x16x32_bf16 v[98:101], v[144:147], v[192:195], v[98:101]
	s_waitcnt lgkmcnt(1)
	v_mfma_f32_16x16x32_bf16 v[82:85], v[144:147], v[200:203], v[82:85]
	v_mfma_f32_16x16x32_bf16 v[82:85], v[140:143], v[196:199], v[82:85]
	v_mfma_f32_16x16x32_bf16 v[74:77], v[148:151], v[196:199], v[74:77]
	v_mfma_f32_16x16x32_bf16 v[74:77], v[152:155], v[200:203], v[74:77]
	v_mfma_f32_16x16x32_bf16 v[90:93], v[152:155], v[192:195], v[90:93]
	v_mfma_f32_16x16x32_bf16 v[90:93], v[148:151], v[188:191], v[90:93]
	v_mfma_f32_16x16x32_bf16 v[106:109], v[148:151], v[180:183], v[106:109]
	v_mfma_f32_16x16x32_bf16 v[106:109], v[152:155], v[184:187], v[106:109]
	s_waitcnt lgkmcnt(0)
	v_mfma_f32_16x16x32_bf16 v[122:125], v[152:155], v[176:179], v[122:125]
	v_mfma_f32_16x16x32_bf16 v[122:125], v[148:151], v[172:175], v[122:125]
	v_mfma_f32_16x16x32_bf16 v[118:121], v[156:159], v[172:175], v[118:121]
	v_mfma_f32_16x16x32_bf16 v[118:121], v[160:163], v[176:179], v[118:121]
	v_mfma_f32_16x16x32_bf16 v[102:105], v[160:163], v[184:187], v[102:105]
	v_mfma_f32_16x16x32_bf16 v[102:105], v[156:159], v[180:183], v[102:105]
	v_mfma_f32_16x16x32_bf16 v[86:89], v[156:159], v[188:191], v[86:89]
	v_mfma_f32_16x16x32_bf16 v[86:89], v[160:163], v[192:195], v[86:89]
	v_mfma_f32_16x16x32_bf16 v[70:73], v[160:163], v[200:203], v[70:73]
	v_mfma_f32_16x16x32_bf16 v[70:73], v[156:159], v[196:199], v[70:73]
	v_mfma_f32_16x16x32_bf16 v[66:69], v[164:167], v[196:199], v[66:69]
	v_mfma_f32_16x16x32_bf16 v[66:69], v[168:171], v[200:203], v[66:69]
	v_mfma_f32_16x16x32_bf16 v[78:81], v[168:171], v[192:195], v[78:81]
	v_mfma_f32_16x16x32_bf16 v[78:81], v[164:167], v[188:191], v[78:81]
	v_mfma_f32_16x16x32_bf16 v[94:97], v[164:167], v[180:183], v[94:97]
	v_mfma_f32_16x16x32_bf16 v[94:97], v[168:171], v[184:187], v[94:97]
	v_mfma_f32_16x16x32_bf16 v[114:117], v[168:171], v[176:179], v[114:117]
	v_mfma_f32_16x16x32_bf16 v[114:117], v[164:167], v[172:175], v[114:117]
	s_barrier
	s_mov_b32 m0, s26
	s_mov_b32 s10, s6
	s_mov_b32 s11, s7
	ds_read_b128 v[172:175], v139 offset:16384
	ds_read_b128 v[176:179], v139 offset:17408
	ds_read_b128 v[180:183], v139 offset:18432
	ds_read_b128 v[184:187], v139 offset:19456
	ds_read_b128 v[188:191], v139 offset:20480
	ds_read_b128 v[192:195], v139 offset:21504
	ds_read_b128 v[196:199], v139 offset:22528
	ds_read_b128 v[200:203], v139 offset:23552
	buffer_load_dwordx4 v135, s[8:11], s54 offen lds
	s_mov_b32 m0, s28
	s_add_i32 s56, s54, 0x80000
	buffer_load_dwordx4 v137, s[8:11], s54 offen lds
	s_mov_b32 m0, s29
	s_nop 0
	buffer_load_dwordx4 v135, s[8:11], s56 offen lds
	s_mov_b32 m0, s30
	s_nop 0
	buffer_load_dwordx4 v137, s[8:11], s56 offen lds
	s_mov_b32 m0, s25
	s_nop 0
	buffer_load_dwordx4 v134, s[4:7], s55 offen lds
	s_mov_b32 m0, s31
	s_nop 0
	buffer_load_dwordx4 v136, s[4:7], s55 offen lds
	s_waitcnt vmcnt(8)
	s_waitcnt lgkmcnt(0)
	s_barrier
	s_waitcnt lgkmcnt(7)
	v_mfma_f32_16x16x32_bf16 v[62:65], v[140:143], v[172:175], v[62:65]
	v_mfma_f32_16x16x32_bf16 v[62:65], v[144:147], v[176:179], v[62:65]
	s_waitcnt lgkmcnt(5)
	v_mfma_f32_16x16x32_bf16 v[46:49], v[144:147], v[184:187], v[46:49]
	v_mfma_f32_16x16x32_bf16 v[46:49], v[140:143], v[180:183], v[46:49]
	s_waitcnt lgkmcnt(3)
	v_mfma_f32_16x16x32_bf16 v[30:33], v[140:143], v[188:191], v[30:33]
	v_mfma_f32_16x16x32_bf16 v[30:33], v[144:147], v[192:195], v[30:33]
	s_waitcnt lgkmcnt(1)
	v_mfma_f32_16x16x32_bf16 v[14:17], v[144:147], v[200:203], v[14:17]
	v_mfma_f32_16x16x32_bf16 v[14:17], v[140:143], v[196:199], v[14:17]
	v_mfma_f32_16x16x32_bf16 v[10:13], v[148:151], v[196:199], v[10:13]
	v_mfma_f32_16x16x32_bf16 v[10:13], v[152:155], v[200:203], v[10:13]
	v_mfma_f32_16x16x32_bf16 v[26:29], v[152:155], v[192:195], v[26:29]
	v_mfma_f32_16x16x32_bf16 v[26:29], v[148:151], v[188:191], v[26:29]
	v_mfma_f32_16x16x32_bf16 v[42:45], v[148:151], v[180:183], v[42:45]
	v_mfma_f32_16x16x32_bf16 v[42:45], v[152:155], v[184:187], v[42:45]
	s_waitcnt lgkmcnt(0)
	v_mfma_f32_16x16x32_bf16 v[58:61], v[152:155], v[176:179], v[58:61]
	v_mfma_f32_16x16x32_bf16 v[58:61], v[148:151], v[172:175], v[58:61]
	v_mfma_f32_16x16x32_bf16 v[54:57], v[156:159], v[172:175], v[54:57]
	v_mfma_f32_16x16x32_bf16 v[54:57], v[160:163], v[176:179], v[54:57]
	v_mfma_f32_16x16x32_bf16 v[38:41], v[160:163], v[184:187], v[38:41]
	v_mfma_f32_16x16x32_bf16 v[38:41], v[156:159], v[180:183], v[38:41]
	v_mfma_f32_16x16x32_bf16 v[22:25], v[156:159], v[188:191], v[22:25]
	v_mfma_f32_16x16x32_bf16 v[22:25], v[160:163], v[192:195], v[22:25]
	v_mfma_f32_16x16x32_bf16 v[6:9], v[160:163], v[200:203], v[6:9]
	v_mfma_f32_16x16x32_bf16 v[6:9], v[156:159], v[196:199], v[6:9]
	v_mfma_f32_16x16x32_bf16 v[2:5], v[164:167], v[196:199], v[2:5]
	v_mfma_f32_16x16x32_bf16 v[2:5], v[168:171], v[200:203], v[2:5]
	v_mfma_f32_16x16x32_bf16 v[18:21], v[168:171], v[192:195], v[18:21]
	v_mfma_f32_16x16x32_bf16 v[18:21], v[164:167], v[188:191], v[18:21]
	v_mfma_f32_16x16x32_bf16 v[34:37], v[164:167], v[180:183], v[34:37]
	v_mfma_f32_16x16x32_bf16 v[34:37], v[168:171], v[184:187], v[34:37]
	v_mfma_f32_16x16x32_bf16 v[50:53], v[168:171], v[176:179], v[50:53]
	v_mfma_f32_16x16x32_bf16 v[50:53], v[164:167], v[172:175], v[50:53]
	s_barrier
	v_add_u32_e32 v152, 0x18000, v138
	v_add_u32_e32 v168, 0x1c000, v138
	ds_read_b128 v[140:143], v152
	ds_read_b128 v[144:147], v152 offset:1024
	ds_read_b128 v[148:151], v152 offset:2048
	ds_read_b128 v[152:155], v152 offset:3072
	ds_read_b128 v[156:159], v168
	ds_read_b128 v[160:163], v168 offset:1024
	ds_read_b128 v[164:167], v168 offset:2048
	ds_read_b128 v[168:171], v168 offset:3072
	s_add_i32 s55, s55, 0x80000
	s_mov_b32 m0, s34
	ds_read_b128 v[172:175], v139 offset:32768
	ds_read_b128 v[176:179], v139 offset:33792
	ds_read_b128 v[180:183], v139 offset:34816
	ds_read_b128 v[184:187], v139 offset:35840
	ds_read_b128 v[188:191], v139 offset:36864
	ds_read_b128 v[192:195], v139 offset:37888
	ds_read_b128 v[196:199], v139 offset:38912
	ds_read_b128 v[200:203], v139 offset:39936
	buffer_load_dwordx4 v134, s[4:7], s55 offen lds
	s_mov_b32 m0, s35
	s_nop 0
	buffer_load_dwordx4 v136, s[4:7], s55 offen lds
	s_waitcnt vmcnt(8)
	s_waitcnt lgkmcnt(0)
	s_barrier
	s_waitcnt lgkmcnt(7)
	v_mfma_f32_16x16x32_bf16 v[126:129], v[140:143], v[172:175], v[126:129]
	v_mfma_f32_16x16x32_bf16 v[126:129], v[144:147], v[176:179], v[126:129]
	s_waitcnt lgkmcnt(5)
	v_mfma_f32_16x16x32_bf16 v[110:113], v[144:147], v[184:187], v[110:113]
	v_mfma_f32_16x16x32_bf16 v[110:113], v[140:143], v[180:183], v[110:113]
	s_waitcnt lgkmcnt(3)
	v_mfma_f32_16x16x32_bf16 v[98:101], v[140:143], v[188:191], v[98:101]
	v_mfma_f32_16x16x32_bf16 v[98:101], v[144:147], v[192:195], v[98:101]
	s_waitcnt lgkmcnt(1)
	v_mfma_f32_16x16x32_bf16 v[82:85], v[144:147], v[200:203], v[82:85]
	v_mfma_f32_16x16x32_bf16 v[82:85], v[140:143], v[196:199], v[82:85]
	v_mfma_f32_16x16x32_bf16 v[74:77], v[148:151], v[196:199], v[74:77]
	v_mfma_f32_16x16x32_bf16 v[74:77], v[152:155], v[200:203], v[74:77]
	v_mfma_f32_16x16x32_bf16 v[90:93], v[152:155], v[192:195], v[90:93]
	v_mfma_f32_16x16x32_bf16 v[90:93], v[148:151], v[188:191], v[90:93]
	v_mfma_f32_16x16x32_bf16 v[106:109], v[148:151], v[180:183], v[106:109]
	v_mfma_f32_16x16x32_bf16 v[106:109], v[152:155], v[184:187], v[106:109]
	s_waitcnt lgkmcnt(0)
	v_mfma_f32_16x16x32_bf16 v[122:125], v[152:155], v[176:179], v[122:125]
	v_mfma_f32_16x16x32_bf16 v[122:125], v[148:151], v[172:175], v[122:125]
	v_mfma_f32_16x16x32_bf16 v[118:121], v[156:159], v[172:175], v[118:121]
	v_mfma_f32_16x16x32_bf16 v[118:121], v[160:163], v[176:179], v[118:121]
	v_mfma_f32_16x16x32_bf16 v[102:105], v[160:163], v[184:187], v[102:105]
	v_mfma_f32_16x16x32_bf16 v[102:105], v[156:159], v[180:183], v[102:105]
	v_mfma_f32_16x16x32_bf16 v[86:89], v[156:159], v[188:191], v[86:89]
	v_mfma_f32_16x16x32_bf16 v[86:89], v[160:163], v[192:195], v[86:89]
	v_mfma_f32_16x16x32_bf16 v[70:73], v[160:163], v[200:203], v[70:73]
	v_mfma_f32_16x16x32_bf16 v[70:73], v[156:159], v[196:199], v[70:73]
	v_mfma_f32_16x16x32_bf16 v[66:69], v[164:167], v[196:199], v[66:69]
	v_mfma_f32_16x16x32_bf16 v[66:69], v[168:171], v[200:203], v[66:69]
	v_mfma_f32_16x16x32_bf16 v[78:81], v[168:171], v[192:195], v[78:81]
	v_mfma_f32_16x16x32_bf16 v[78:81], v[164:167], v[188:191], v[78:81]
	v_mfma_f32_16x16x32_bf16 v[94:97], v[164:167], v[180:183], v[94:97]
	v_mfma_f32_16x16x32_bf16 v[94:97], v[168:171], v[184:187], v[94:97]
	v_mfma_f32_16x16x32_bf16 v[114:117], v[168:171], v[176:179], v[114:117]
	v_mfma_f32_16x16x32_bf16 v[114:117], v[164:167], v[172:175], v[114:117]
	s_barrier
	s_mov_b32 m0, s36
	s_or_b32 s55, s54, 0x80
	ds_read_b128 v[172:175], v139 offset:49152
	ds_read_b128 v[176:179], v139 offset:50176
	ds_read_b128 v[180:183], v139 offset:51200
	ds_read_b128 v[184:187], v139 offset:52224
	ds_read_b128 v[188:191], v139 offset:53248
	ds_read_b128 v[192:195], v139 offset:54272
	ds_read_b128 v[196:199], v139 offset:55296
	ds_read_b128 v[200:203], v139 offset:56320
	buffer_load_dwordx4 v135, s[8:11], s55 offen lds
	s_mov_b32 m0, s37
	s_add_i32 s54, s54, 0x80080
	buffer_load_dwordx4 v137, s[8:11], s55 offen lds
	s_mov_b32 m0, s41
	s_nop 0
	buffer_load_dwordx4 v135, s[8:11], s54 offen lds
	s_mov_b32 m0, s42
	s_nop 0
	buffer_load_dwordx4 v137, s[8:11], s54 offen lds
	s_mov_b32 m0, s38
	s_nop 0
	buffer_load_dwordx4 v134, s[4:7], s53 offen lds
	s_mov_b32 m0, s40
	s_nop 0
	buffer_load_dwordx4 v136, s[4:7], s53 offen lds
	s_waitcnt vmcnt(8)
	s_waitcnt lgkmcnt(0)
	s_barrier
	s_waitcnt lgkmcnt(7)
	v_mfma_f32_16x16x32_bf16 v[62:65], v[140:143], v[172:175], v[62:65]
	v_mfma_f32_16x16x32_bf16 v[62:65], v[144:147], v[176:179], v[62:65]
	s_waitcnt lgkmcnt(5)
	v_mfma_f32_16x16x32_bf16 v[46:49], v[144:147], v[184:187], v[46:49]
	v_mfma_f32_16x16x32_bf16 v[46:49], v[140:143], v[180:183], v[46:49]
	s_waitcnt lgkmcnt(3)
	v_mfma_f32_16x16x32_bf16 v[30:33], v[140:143], v[188:191], v[30:33]
	v_mfma_f32_16x16x32_bf16 v[30:33], v[144:147], v[192:195], v[30:33]
	s_waitcnt lgkmcnt(1)
	v_mfma_f32_16x16x32_bf16 v[14:17], v[144:147], v[200:203], v[14:17]
	v_mfma_f32_16x16x32_bf16 v[14:17], v[140:143], v[196:199], v[14:17]
	v_mfma_f32_16x16x32_bf16 v[10:13], v[148:151], v[196:199], v[10:13]
	v_mfma_f32_16x16x32_bf16 v[10:13], v[152:155], v[200:203], v[10:13]
	v_mfma_f32_16x16x32_bf16 v[26:29], v[152:155], v[192:195], v[26:29]
	v_mfma_f32_16x16x32_bf16 v[26:29], v[148:151], v[188:191], v[26:29]
	v_mfma_f32_16x16x32_bf16 v[42:45], v[148:151], v[180:183], v[42:45]
	v_mfma_f32_16x16x32_bf16 v[42:45], v[152:155], v[184:187], v[42:45]
	s_waitcnt lgkmcnt(0)
	v_mfma_f32_16x16x32_bf16 v[58:61], v[152:155], v[176:179], v[58:61]
	v_mfma_f32_16x16x32_bf16 v[58:61], v[148:151], v[172:175], v[58:61]
	v_mfma_f32_16x16x32_bf16 v[54:57], v[156:159], v[172:175], v[54:57]
	v_mfma_f32_16x16x32_bf16 v[54:57], v[160:163], v[176:179], v[54:57]
	v_mfma_f32_16x16x32_bf16 v[38:41], v[160:163], v[184:187], v[38:41]
	v_mfma_f32_16x16x32_bf16 v[38:41], v[156:159], v[180:183], v[38:41]
	v_mfma_f32_16x16x32_bf16 v[22:25], v[156:159], v[188:191], v[22:25]
	v_mfma_f32_16x16x32_bf16 v[22:25], v[160:163], v[192:195], v[22:25]
	v_mfma_f32_16x16x32_bf16 v[6:9], v[160:163], v[200:203], v[6:9]
	v_mfma_f32_16x16x32_bf16 v[6:9], v[156:159], v[196:199], v[6:9]
	v_mfma_f32_16x16x32_bf16 v[2:5], v[164:167], v[196:199], v[2:5]
	v_mfma_f32_16x16x32_bf16 v[2:5], v[168:171], v[200:203], v[2:5]
	v_mfma_f32_16x16x32_bf16 v[18:21], v[168:171], v[192:195], v[18:21]
	v_mfma_f32_16x16x32_bf16 v[18:21], v[164:167], v[188:191], v[18:21]
	v_mfma_f32_16x16x32_bf16 v[34:37], v[164:167], v[180:183], v[34:37]
	v_mfma_f32_16x16x32_bf16 v[34:37], v[168:171], v[184:187], v[34:37]
	v_mfma_f32_16x16x32_bf16 v[50:53], v[168:171], v[176:179], v[50:53]
	v_mfma_f32_16x16x32_bf16 v[50:53], v[164:167], v[172:175], v[50:53]
	s_barrier
	s_add_i32 s51, s51, 2
	s_addk_i32 s52, 0x100
	s_cmp_gt_u32 s51, 29
	s_cbranch_scc0 .LBB0_686
	s_andn2_b64 vcc, exec, s[2:3]
	s_cbranch_vccnz .LBB0_678
	v_mov_b32_e32 v2, 0
	s_mov_b32 s14, s46
	s_mov_b32 s15, s47
	s_mov_b32 s27, s48
	s_mov_b32 s33, s13
	s_mov_b32 s45, s12
	v_mov_b32_e32 v3, v2
	v_mov_b32_e32 v4, v2
	v_mov_b32_e32 v5, v2
	v_mov_b32_e32 v6, v2
	v_mov_b32_e32 v7, v2
	v_mov_b32_e32 v8, v2
	v_mov_b32_e32 v9, v2
	v_mov_b32_e32 v18, v2
	v_mov_b32_e32 v19, v2
	v_mov_b32_e32 v20, v2
	v_mov_b32_e32 v21, v2
	v_mov_b32_e32 v22, v2
	v_mov_b32_e32 v23, v2
	v_mov_b32_e32 v24, v2
	v_mov_b32_e32 v25, v2
	v_mov_b32_e32 v34, v2
	v_mov_b32_e32 v35, v2
	v_mov_b32_e32 v36, v2
	v_mov_b32_e32 v37, v2
	v_mov_b32_e32 v38, v2
	v_mov_b32_e32 v39, v2
	v_mov_b32_e32 v40, v2
	v_mov_b32_e32 v41, v2
	v_mov_b32_e32 v50, v2
	v_mov_b32_e32 v51, v2
	v_mov_b32_e32 v52, v2
	v_mov_b32_e32 v53, v2
	v_mov_b32_e32 v54, v2
	v_mov_b32_e32 v55, v2
	v_mov_b32_e32 v56, v2
	v_mov_b32_e32 v57, v2
	v_mov_b32_e32 v10, v2
	v_mov_b32_e32 v11, v2
	v_mov_b32_e32 v12, v2
	v_mov_b32_e32 v13, v2
	v_mov_b32_e32 v14, v2
	v_mov_b32_e32 v15, v2
	v_mov_b32_e32 v16, v2
	v_mov_b32_e32 v17, v2
	v_mov_b32_e32 v26, v2
	v_mov_b32_e32 v27, v2
	v_mov_b32_e32 v28, v2
	v_mov_b32_e32 v29, v2
	v_mov_b32_e32 v30, v2
	v_mov_b32_e32 v31, v2
	v_mov_b32_e32 v32, v2
	v_mov_b32_e32 v33, v2
	v_mov_b32_e32 v42, v2
	v_mov_b32_e32 v43, v2
	v_mov_b32_e32 v44, v2
	v_mov_b32_e32 v45, v2
	v_mov_b32_e32 v46, v2
	v_mov_b32_e32 v47, v2
	v_mov_b32_e32 v48, v2
	v_mov_b32_e32 v49, v2
	v_mov_b32_e32 v58, v2
	v_mov_b32_e32 v59, v2
	v_mov_b32_e32 v60, v2
	v_mov_b32_e32 v61, v2
	v_mov_b32_e32 v62, v2
	v_mov_b32_e32 v63, v2
	v_mov_b32_e32 v64, v2
	v_mov_b32_e32 v65, v2
	v_mov_b32_e32 v66, v2
	v_mov_b32_e32 v67, v2
	v_mov_b32_e32 v68, v2
	v_mov_b32_e32 v69, v2
	v_mov_b32_e32 v70, v2
	v_mov_b32_e32 v71, v2
	v_mov_b32_e32 v72, v2
	v_mov_b32_e32 v73, v2
	v_mov_b32_e32 v78, v2
	v_mov_b32_e32 v79, v2
	v_mov_b32_e32 v80, v2
	v_mov_b32_e32 v81, v2
	v_mov_b32_e32 v86, v2
	v_mov_b32_e32 v87, v2
	v_mov_b32_e32 v88, v2
	v_mov_b32_e32 v89, v2
	v_mov_b32_e32 v94, v2
	v_mov_b32_e32 v95, v2
	v_mov_b32_e32 v96, v2
	v_mov_b32_e32 v97, v2
	v_mov_b32_e32 v102, v2
	v_mov_b32_e32 v103, v2
	v_mov_b32_e32 v104, v2
	v_mov_b32_e32 v105, v2
	v_mov_b32_e32 v114, v2
	v_mov_b32_e32 v115, v2
	v_mov_b32_e32 v116, v2
	v_mov_b32_e32 v117, v2
	v_mov_b32_e32 v118, v2
	v_mov_b32_e32 v119, v2
	v_mov_b32_e32 v120, v2
	v_mov_b32_e32 v121, v2
	v_mov_b32_e32 v74, v2
	v_mov_b32_e32 v75, v2
	v_mov_b32_e32 v76, v2
	v_mov_b32_e32 v77, v2
	v_mov_b32_e32 v82, v2
	v_mov_b32_e32 v83, v2
	v_mov_b32_e32 v84, v2
	v_mov_b32_e32 v85, v2
	v_mov_b32_e32 v90, v2
	v_mov_b32_e32 v91, v2
	v_mov_b32_e32 v92, v2
	v_mov_b32_e32 v93, v2
	v_mov_b32_e32 v98, v2
	v_mov_b32_e32 v99, v2
	v_mov_b32_e32 v100, v2
	v_mov_b32_e32 v101, v2
	v_mov_b32_e32 v106, v2
	v_mov_b32_e32 v107, v2
	v_mov_b32_e32 v108, v2
	v_mov_b32_e32 v109, v2
	v_mov_b32_e32 v110, v2
	v_mov_b32_e32 v111, v2
	v_mov_b32_e32 v112, v2
	v_mov_b32_e32 v113, v2
	v_mov_b32_e32 v122, v2
	v_mov_b32_e32 v123, v2
	v_mov_b32_e32 v124, v2
	v_mov_b32_e32 v125, v2
	v_mov_b32_e32 v126, v2
	v_mov_b32_e32 v127, v2
	v_mov_b32_e32 v128, v2
	v_mov_b32_e32 v129, v2
	s_branch .LBB0_678

.LBB0_907:
	v_add_u32_e32 v166, 0x10000, v179
	ds_read_b128 v[162:165], v166
	ds_read_b128 v[182:185], v166 offset:1024
	ds_read_b128 v[186:189], v166 offset:2048
	ds_read_b128 v[190:193], v166 offset:3072
	v_add_u32_e32 v166, 0x14000, v179
	ds_read_b128 v[194:197], v166
	ds_read_b128 v[198:201], v166 offset:1024
	ds_read_b128 v[202:205], v166 offset:2048
	ds_read_b128 v[206:209], v166 offset:3072
	s_add_i32 s10, s45, s64
	s_add_i32 s26, s40, s64
	s_add_i32 s11, s10, 0x1000
	s_addk_i32 s26, 0x1000
	s_cmp_eq_u32 s64, 0
	s_cselect_b32 s29, s62, s11
	s_cselect_b32 s27, s63, s26
	s_add_i32 s26, s29, 0x80
	s_add_i32 s28, s27, 0x80
	s_add_i32 s10, s10, 0x80f80
	s_mov_b32 m0, s55
	ds_read_b128 v[210:213], v180
	ds_read_b128 v[214:217], v180 offset:1024
	ds_read_b128 v[218:221], v180 offset:2048
	ds_read_b128 v[222:225], v180 offset:3072
	ds_read_b128 v[226:229], v180 offset:4096
	ds_read_b128 v[230:233], v180 offset:5120
	ds_read_b128 v[234:237], v180 offset:6144
	ds_read_b128 v[238:241], v180 offset:7168
	buffer_load_dwordx4 v1, s[4:7], s10 offen lds
	s_mov_b32 m0, s56
	s_nop 0
	buffer_load_dwordx4 v175, s[4:7], s10 offen lds
	s_waitcnt vmcnt(8)
	s_waitcnt lgkmcnt(0)
	s_barrier
	s_waitcnt lgkmcnt(7)
	v_mfma_f32_16x16x32_bf16 v[126:129], v[162:165], v[210:213], v[126:129]
	v_mfma_f32_16x16x32_bf16 v[126:129], v[182:185], v[214:217], v[126:129]
	s_waitcnt lgkmcnt(5)
	v_mfma_f32_16x16x32_bf16 v[118:121], v[182:185], v[222:225], v[118:121]
	v_mfma_f32_16x16x32_bf16 v[118:121], v[162:165], v[218:221], v[118:121]
	s_waitcnt lgkmcnt(3)
	v_mfma_f32_16x16x32_bf16 v[110:113], v[162:165], v[226:229], v[110:113]
	v_mfma_f32_16x16x32_bf16 v[110:113], v[182:185], v[230:233], v[110:113]
	s_waitcnt lgkmcnt(1)
	v_mfma_f32_16x16x32_bf16 v[102:105], v[182:185], v[238:241], v[102:105]
	v_mfma_f32_16x16x32_bf16 v[102:105], v[162:165], v[234:237], v[102:105]
	v_mfma_f32_16x16x32_bf16 v[98:101], v[186:189], v[234:237], v[98:101]
	v_mfma_f32_16x16x32_bf16 v[98:101], v[190:193], v[238:241], v[98:101]
	v_mfma_f32_16x16x32_bf16 v[106:109], v[190:193], v[230:233], v[106:109]
	v_mfma_f32_16x16x32_bf16 v[106:109], v[186:189], v[226:229], v[106:109]
	v_mfma_f32_16x16x32_bf16 v[114:117], v[186:189], v[218:221], v[114:117]
	v_mfma_f32_16x16x32_bf16 v[114:117], v[190:193], v[222:225], v[114:117]
	s_waitcnt lgkmcnt(0)
	v_mfma_f32_16x16x32_bf16 v[122:125], v[190:193], v[214:217], v[122:125]
	v_mfma_f32_16x16x32_bf16 v[122:125], v[186:189], v[210:213], v[122:125]
	v_mfma_f32_16x16x32_bf16 v[94:97], v[194:197], v[210:213], v[94:97]
	v_mfma_f32_16x16x32_bf16 v[94:97], v[198:201], v[214:217], v[94:97]
	v_mfma_f32_16x16x32_bf16 v[86:89], v[198:201], v[222:225], v[86:89]
	v_mfma_f32_16x16x32_bf16 v[86:89], v[194:197], v[218:221], v[86:89]
	v_mfma_f32_16x16x32_bf16 v[78:81], v[194:197], v[226:229], v[78:81]
	v_mfma_f32_16x16x32_bf16 v[78:81], v[198:201], v[230:233], v[78:81]
	v_mfma_f32_16x16x32_bf16 v[70:73], v[198:201], v[238:241], v[70:73]
	v_mfma_f32_16x16x32_bf16 v[70:73], v[194:197], v[234:237], v[70:73]
	v_mfma_f32_16x16x32_bf16 v[66:69], v[202:205], v[234:237], v[66:69]
	v_mfma_f32_16x16x32_bf16 v[66:69], v[206:209], v[238:241], v[66:69]
	v_mfma_f32_16x16x32_bf16 v[74:77], v[206:209], v[230:233], v[74:77]
	v_mfma_f32_16x16x32_bf16 v[74:77], v[202:205], v[226:229], v[74:77]
	v_mfma_f32_16x16x32_bf16 v[82:85], v[202:205], v[218:221], v[82:85]
	v_mfma_f32_16x16x32_bf16 v[82:85], v[206:209], v[222:225], v[82:85]
	v_mfma_f32_16x16x32_bf16 v[90:93], v[206:209], v[214:217], v[90:93]
	v_mfma_f32_16x16x32_bf16 v[90:93], v[202:205], v[210:213], v[90:93]
	s_barrier
	s_mov_b32 m0, s37
	s_mov_b32 s10, s6
	s_mov_b32 s11, s7
	ds_read_b128 v[210:213], v180 offset:16384
	ds_read_b128 v[214:217], v180 offset:17408
	ds_read_b128 v[218:221], v180 offset:18432
	ds_read_b128 v[222:225], v180 offset:19456
	ds_read_b128 v[226:229], v180 offset:20480
	ds_read_b128 v[230:233], v180 offset:21504
	ds_read_b128 v[234:237], v180 offset:22528
	ds_read_b128 v[238:241], v180 offset:23552
	buffer_load_dwordx4 v174, s[8:11], s27 offen lds
	s_mov_b32 m0, s38
	s_add_i32 s66, s27, 0x80000
	buffer_load_dwordx4 v176, s[8:11], s27 offen lds
	s_mov_b32 m0, s39
	s_nop 0
	buffer_load_dwordx4 v174, s[8:11], s66 offen lds
	s_mov_b32 m0, s41
	s_nop 0
	buffer_load_dwordx4 v176, s[8:11], s66 offen lds
	s_mov_b32 m0, s36
	s_nop 0
	buffer_load_dwordx4 v1, s[4:7], s29 offen lds
	s_mov_b32 m0, s42
	s_nop 0
	buffer_load_dwordx4 v175, s[4:7], s29 offen lds
	s_waitcnt vmcnt(8)
	s_waitcnt lgkmcnt(0)
	s_barrier
	s_waitcnt lgkmcnt(7)
	v_mfma_f32_16x16x32_bf16 v[62:65], v[162:165], v[210:213], v[62:65]
	v_mfma_f32_16x16x32_bf16 v[62:65], v[182:185], v[214:217], v[62:65]
	s_waitcnt lgkmcnt(5)
	v_mfma_f32_16x16x32_bf16 v[54:57], v[182:185], v[222:225], v[54:57]
	v_mfma_f32_16x16x32_bf16 v[54:57], v[162:165], v[218:221], v[54:57]
	s_waitcnt lgkmcnt(3)
	v_mfma_f32_16x16x32_bf16 v[46:49], v[162:165], v[226:229], v[46:49]
	v_mfma_f32_16x16x32_bf16 v[46:49], v[182:185], v[230:233], v[46:49]
	s_waitcnt lgkmcnt(1)
	v_mfma_f32_16x16x32_bf16 v[38:41], v[182:185], v[238:241], v[38:41]
	v_mfma_f32_16x16x32_bf16 v[38:41], v[162:165], v[234:237], v[38:41]
	v_mfma_f32_16x16x32_bf16 v[34:37], v[186:189], v[234:237], v[34:37]
	v_mfma_f32_16x16x32_bf16 v[34:37], v[190:193], v[238:241], v[34:37]
	v_mfma_f32_16x16x32_bf16 v[42:45], v[190:193], v[230:233], v[42:45]
	v_mfma_f32_16x16x32_bf16 v[42:45], v[186:189], v[226:229], v[42:45]
	v_mfma_f32_16x16x32_bf16 v[50:53], v[186:189], v[218:221], v[50:53]
	v_mfma_f32_16x16x32_bf16 v[50:53], v[190:193], v[222:225], v[50:53]
	s_waitcnt lgkmcnt(0)
	v_mfma_f32_16x16x32_bf16 v[58:61], v[190:193], v[214:217], v[58:61]
	v_mfma_f32_16x16x32_bf16 v[58:61], v[186:189], v[210:213], v[58:61]
	v_mfma_f32_16x16x32_bf16 v[30:33], v[194:197], v[210:213], v[30:33]
	v_mfma_f32_16x16x32_bf16 v[30:33], v[198:201], v[214:217], v[30:33]
	v_mfma_f32_16x16x32_bf16 v[22:25], v[198:201], v[222:225], v[22:25]
	v_mfma_f32_16x16x32_bf16 v[22:25], v[194:197], v[218:221], v[22:25]
	v_mfma_f32_16x16x32_bf16 v[14:17], v[194:197], v[226:229], v[14:17]
	v_mfma_f32_16x16x32_bf16 v[14:17], v[198:201], v[230:233], v[14:17]
	v_mfma_f32_16x16x32_bf16 v[6:9], v[198:201], v[238:241], v[6:9]
	v_mfma_f32_16x16x32_bf16 v[6:9], v[194:197], v[234:237], v[6:9]
	v_mfma_f32_16x16x32_bf16 v[2:5], v[202:205], v[234:237], v[2:5]
	v_mfma_f32_16x16x32_bf16 v[2:5], v[206:209], v[238:241], v[2:5]
	v_mfma_f32_16x16x32_bf16 v[10:13], v[206:209], v[230:233], v[10:13]
	v_mfma_f32_16x16x32_bf16 v[10:13], v[202:205], v[226:229], v[10:13]
	v_mfma_f32_16x16x32_bf16 v[18:21], v[202:205], v[218:221], v[18:21]
	v_mfma_f32_16x16x32_bf16 v[18:21], v[206:209], v[222:225], v[18:21]
	v_mfma_f32_16x16x32_bf16 v[26:29], v[206:209], v[214:217], v[26:29]
	v_mfma_f32_16x16x32_bf16 v[26:29], v[202:205], v[210:213], v[26:29]
	s_barrier
	v_add_u32_e32 v166, 0x18000, v179
	ds_read_b128 v[162:165], v166
	ds_read_b128 v[182:185], v166 offset:1024
	ds_read_b128 v[186:189], v166 offset:2048
	ds_read_b128 v[190:193], v166 offset:3072
	v_add_u32_e32 v166, 0x1c000, v179
	ds_read_b128 v[194:197], v166
	ds_read_b128 v[198:201], v166 offset:1024
	ds_read_b128 v[202:205], v166 offset:2048
	ds_read_b128 v[206:209], v166 offset:3072
	s_add_i32 s29, s29, 0x80000
	s_mov_b32 m0, s43
	ds_read_b128 v[210:213], v180 offset:32768
	ds_read_b128 v[214:217], v180 offset:33792
	ds_read_b128 v[218:221], v180 offset:34816
	ds_read_b128 v[222:225], v180 offset:35840
	ds_read_b128 v[226:229], v180 offset:36864
	ds_read_b128 v[230:233], v180 offset:37888
	ds_read_b128 v[234:237], v180 offset:38912
	ds_read_b128 v[238:241], v180 offset:39936
	buffer_load_dwordx4 v1, s[4:7], s29 offen lds
	s_mov_b32 m0, s44
	s_nop 0
	buffer_load_dwordx4 v175, s[4:7], s29 offen lds
	s_waitcnt vmcnt(8)
	s_waitcnt lgkmcnt(0)
	s_barrier
	s_waitcnt lgkmcnt(7)
	v_mfma_f32_16x16x32_bf16 v[126:129], v[162:165], v[210:213], v[126:129]
	v_mfma_f32_16x16x32_bf16 v[126:129], v[182:185], v[214:217], v[126:129]
	s_waitcnt lgkmcnt(5)
	v_mfma_f32_16x16x32_bf16 v[118:121], v[182:185], v[222:225], v[118:121]
	v_mfma_f32_16x16x32_bf16 v[118:121], v[162:165], v[218:221], v[118:121]
	s_waitcnt lgkmcnt(3)
	v_mfma_f32_16x16x32_bf16 v[110:113], v[162:165], v[226:229], v[110:113]
	v_mfma_f32_16x16x32_bf16 v[110:113], v[182:185], v[230:233], v[110:113]
	s_waitcnt lgkmcnt(1)
	v_mfma_f32_16x16x32_bf16 v[102:105], v[182:185], v[238:241], v[102:105]
	v_mfma_f32_16x16x32_bf16 v[102:105], v[162:165], v[234:237], v[102:105]
	v_mfma_f32_16x16x32_bf16 v[98:101], v[186:189], v[234:237], v[98:101]
	v_mfma_f32_16x16x32_bf16 v[98:101], v[190:193], v[238:241], v[98:101]
	v_mfma_f32_16x16x32_bf16 v[106:109], v[190:193], v[230:233], v[106:109]
	v_mfma_f32_16x16x32_bf16 v[106:109], v[186:189], v[226:229], v[106:109]
	v_mfma_f32_16x16x32_bf16 v[114:117], v[186:189], v[218:221], v[114:117]
	v_mfma_f32_16x16x32_bf16 v[114:117], v[190:193], v[222:225], v[114:117]
	s_waitcnt lgkmcnt(0)
	v_mfma_f32_16x16x32_bf16 v[122:125], v[190:193], v[214:217], v[122:125]
	v_mfma_f32_16x16x32_bf16 v[122:125], v[186:189], v[210:213], v[122:125]
	v_mfma_f32_16x16x32_bf16 v[94:97], v[194:197], v[210:213], v[94:97]
	v_mfma_f32_16x16x32_bf16 v[94:97], v[198:201], v[214:217], v[94:97]
	v_mfma_f32_16x16x32_bf16 v[86:89], v[198:201], v[222:225], v[86:89]
	v_mfma_f32_16x16x32_bf16 v[86:89], v[194:197], v[218:221], v[86:89]
	v_mfma_f32_16x16x32_bf16 v[78:81], v[194:197], v[226:229], v[78:81]
	v_mfma_f32_16x16x32_bf16 v[78:81], v[198:201], v[230:233], v[78:81]
	v_mfma_f32_16x16x32_bf16 v[70:73], v[198:201], v[238:241], v[70:73]
	v_mfma_f32_16x16x32_bf16 v[70:73], v[194:197], v[234:237], v[70:73]
	v_mfma_f32_16x16x32_bf16 v[66:69], v[202:205], v[234:237], v[66:69]
	v_mfma_f32_16x16x32_bf16 v[66:69], v[206:209], v[238:241], v[66:69]
	v_mfma_f32_16x16x32_bf16 v[74:77], v[206:209], v[230:233], v[74:77]
	v_mfma_f32_16x16x32_bf16 v[74:77], v[202:205], v[226:229], v[74:77]
	v_mfma_f32_16x16x32_bf16 v[82:85], v[202:205], v[218:221], v[82:85]
	v_mfma_f32_16x16x32_bf16 v[82:85], v[206:209], v[222:225], v[82:85]
	v_mfma_f32_16x16x32_bf16 v[90:93], v[206:209], v[214:217], v[90:93]
	v_mfma_f32_16x16x32_bf16 v[90:93], v[202:205], v[210:213], v[90:93]
	s_barrier
	s_mov_b32 m0, s49
	ds_read_b128 v[210:213], v180 offset:49152
	ds_read_b128 v[214:217], v180 offset:50176
	ds_read_b128 v[218:221], v180 offset:51200
	ds_read_b128 v[222:225], v180 offset:52224
	ds_read_b128 v[226:229], v180 offset:53248
	ds_read_b128 v[230:233], v180 offset:54272
	ds_read_b128 v[234:237], v180 offset:55296
	ds_read_b128 v[238:241], v180 offset:56320
	buffer_load_dwordx4 v174, s[8:11], s28 offen lds
	s_mov_b32 m0, s50
	s_add_i32 s27, s27, 0x80080
	buffer_load_dwordx4 v176, s[8:11], s28 offen lds
	s_mov_b32 m0, s53
	s_nop 0
	buffer_load_dwordx4 v174, s[8:11], s27 offen lds
	s_mov_b32 m0, s54
	s_nop 0
	buffer_load_dwordx4 v176, s[8:11], s27 offen lds
	s_mov_b32 m0, s51
	s_nop 0
	buffer_load_dwordx4 v1, s[4:7], s26 offen lds
	s_mov_b32 m0, s52
	s_nop 0
	buffer_load_dwordx4 v175, s[4:7], s26 offen lds
	s_waitcnt vmcnt(8)
	s_waitcnt lgkmcnt(0)
	s_barrier
	s_waitcnt lgkmcnt(7)
	v_mfma_f32_16x16x32_bf16 v[62:65], v[162:165], v[210:213], v[62:65]
	v_mfma_f32_16x16x32_bf16 v[62:65], v[182:185], v[214:217], v[62:65]
	s_waitcnt lgkmcnt(5)
	v_mfma_f32_16x16x32_bf16 v[54:57], v[182:185], v[222:225], v[54:57]
	v_mfma_f32_16x16x32_bf16 v[54:57], v[162:165], v[218:221], v[54:57]
	s_waitcnt lgkmcnt(3)
	v_mfma_f32_16x16x32_bf16 v[46:49], v[162:165], v[226:229], v[46:49]
	v_mfma_f32_16x16x32_bf16 v[46:49], v[182:185], v[230:233], v[46:49]
	s_waitcnt lgkmcnt(1)
	v_mfma_f32_16x16x32_bf16 v[38:41], v[182:185], v[238:241], v[38:41]
	v_mfma_f32_16x16x32_bf16 v[38:41], v[162:165], v[234:237], v[38:41]
	v_mfma_f32_16x16x32_bf16 v[34:37], v[186:189], v[234:237], v[34:37]
	v_mfma_f32_16x16x32_bf16 v[34:37], v[190:193], v[238:241], v[34:37]
	v_mfma_f32_16x16x32_bf16 v[42:45], v[190:193], v[230:233], v[42:45]
	v_mfma_f32_16x16x32_bf16 v[42:45], v[186:189], v[226:229], v[42:45]
	v_mfma_f32_16x16x32_bf16 v[50:53], v[186:189], v[218:221], v[50:53]
	v_mfma_f32_16x16x32_bf16 v[50:53], v[190:193], v[222:225], v[50:53]
	s_waitcnt lgkmcnt(0)
	v_mfma_f32_16x16x32_bf16 v[58:61], v[190:193], v[214:217], v[58:61]
	v_mfma_f32_16x16x32_bf16 v[58:61], v[186:189], v[210:213], v[58:61]
	v_mfma_f32_16x16x32_bf16 v[30:33], v[194:197], v[210:213], v[30:33]
	v_mfma_f32_16x16x32_bf16 v[30:33], v[198:201], v[214:217], v[30:33]
	v_mfma_f32_16x16x32_bf16 v[22:25], v[198:201], v[222:225], v[22:25]
	v_mfma_f32_16x16x32_bf16 v[22:25], v[194:197], v[218:221], v[22:25]
	v_mfma_f32_16x16x32_bf16 v[14:17], v[194:197], v[226:229], v[14:17]
	v_mfma_f32_16x16x32_bf16 v[14:17], v[198:201], v[230:233], v[14:17]
	v_mfma_f32_16x16x32_bf16 v[6:9], v[198:201], v[238:241], v[6:9]
	v_mfma_f32_16x16x32_bf16 v[6:9], v[194:197], v[234:237], v[6:9]
	v_mfma_f32_16x16x32_bf16 v[2:5], v[202:205], v[234:237], v[2:5]
	v_mfma_f32_16x16x32_bf16 v[2:5], v[206:209], v[238:241], v[2:5]
	v_mfma_f32_16x16x32_bf16 v[10:13], v[206:209], v[230:233], v[10:13]
	v_mfma_f32_16x16x32_bf16 v[10:13], v[202:205], v[226:229], v[10:13]
	v_mfma_f32_16x16x32_bf16 v[18:21], v[202:205], v[218:221], v[18:21]
	v_mfma_f32_16x16x32_bf16 v[18:21], v[206:209], v[222:225], v[18:21]
	v_mfma_f32_16x16x32_bf16 v[26:29], v[206:209], v[214:217], v[26:29]
	v_mfma_f32_16x16x32_bf16 v[26:29], v[202:205], v[210:213], v[26:29]
	s_barrier
	s_add_i32 s10, s65, 2
	s_addk_i32 s64, 0x100
	s_cmp_gt_u32 s65, 29
	s_cbranch_scc1 .LBB0_910
	s_mov_b32 s65, s10
	s_branch .LBB0_869

.LBB0_1029:
	v_add_u32_e32 v152, 0x10000, v138
	v_add_u32_e32 v168, 0x14000, v138
	ds_read_b128 v[140:143], v152
	ds_read_b128 v[144:147], v152 offset:1024
	ds_read_b128 v[148:151], v152 offset:2048
	ds_read_b128 v[152:155], v152 offset:3072
	ds_read_b128 v[156:159], v168
	ds_read_b128 v[160:163], v168 offset:1024
	ds_read_b128 v[164:167], v168 offset:2048
	ds_read_b128 v[168:171], v168 offset:3072
	s_add_i32 s10, s30, s50
	s_add_i32 s51, s25, s50
	s_add_i32 s11, s10, 0x4000
	s_addk_i32 s51, 0x4000
	s_cmp_eq_u32 s50, 0
	s_cselect_b32 s53, s47, s11
	s_cselect_b32 s52, s48, s51
	s_or_b32 s51, s53, 0x80
	s_add_i32 s10, s10, 0x203f80
	s_mov_b32 m0, s41
	ds_read_b128 v[172:175], v139
	ds_read_b128 v[176:179], v139 offset:1024
	ds_read_b128 v[180:183], v139 offset:2048
	ds_read_b128 v[184:187], v139 offset:3072
	ds_read_b128 v[188:191], v139 offset:4096
	ds_read_b128 v[192:195], v139 offset:5120
	ds_read_b128 v[196:199], v139 offset:6144
	ds_read_b128 v[200:203], v139 offset:7168
	buffer_load_dwordx4 v134, s[4:7], s10 offen lds
	s_mov_b32 m0, s42
	s_nop 0
	buffer_load_dwordx4 v136, s[4:7], s10 offen lds
	s_waitcnt vmcnt(8)
	s_waitcnt lgkmcnt(0)
	s_barrier
	s_waitcnt lgkmcnt(7)
	v_mfma_f32_16x16x32_bf16 v[126:129], v[140:143], v[172:175], v[126:129]
	v_mfma_f32_16x16x32_bf16 v[126:129], v[144:147], v[176:179], v[126:129]
	s_waitcnt lgkmcnt(5)
	v_mfma_f32_16x16x32_bf16 v[114:117], v[144:147], v[184:187], v[114:117]
	v_mfma_f32_16x16x32_bf16 v[114:117], v[140:143], v[180:183], v[114:117]
	s_waitcnt lgkmcnt(3)
	v_mfma_f32_16x16x32_bf16 v[98:101], v[140:143], v[188:191], v[98:101]
	v_mfma_f32_16x16x32_bf16 v[98:101], v[144:147], v[192:195], v[98:101]
	s_waitcnt lgkmcnt(1)
	v_mfma_f32_16x16x32_bf16 v[82:85], v[144:147], v[200:203], v[82:85]
	v_mfma_f32_16x16x32_bf16 v[82:85], v[140:143], v[196:199], v[82:85]
	v_mfma_f32_16x16x32_bf16 v[74:77], v[148:151], v[196:199], v[74:77]
	v_mfma_f32_16x16x32_bf16 v[74:77], v[152:155], v[200:203], v[74:77]
	v_mfma_f32_16x16x32_bf16 v[90:93], v[152:155], v[192:195], v[90:93]
	v_mfma_f32_16x16x32_bf16 v[90:93], v[148:151], v[188:191], v[90:93]
	v_mfma_f32_16x16x32_bf16 v[106:109], v[148:151], v[180:183], v[106:109]
	v_mfma_f32_16x16x32_bf16 v[106:109], v[152:155], v[184:187], v[106:109]
	s_waitcnt lgkmcnt(0)
	v_mfma_f32_16x16x32_bf16 v[122:125], v[152:155], v[176:179], v[122:125]
	v_mfma_f32_16x16x32_bf16 v[122:125], v[148:151], v[172:175], v[122:125]
	v_mfma_f32_16x16x32_bf16 v[118:121], v[156:159], v[172:175], v[118:121]
	v_mfma_f32_16x16x32_bf16 v[118:121], v[160:163], v[176:179], v[118:121]
	v_mfma_f32_16x16x32_bf16 v[102:105], v[160:163], v[184:187], v[102:105]
	v_mfma_f32_16x16x32_bf16 v[102:105], v[156:159], v[180:183], v[102:105]
	v_mfma_f32_16x16x32_bf16 v[86:89], v[156:159], v[188:191], v[86:89]
	v_mfma_f32_16x16x32_bf16 v[86:89], v[160:163], v[192:195], v[86:89]
	v_mfma_f32_16x16x32_bf16 v[70:73], v[160:163], v[200:203], v[70:73]
	v_mfma_f32_16x16x32_bf16 v[70:73], v[156:159], v[196:199], v[70:73]
	v_mfma_f32_16x16x32_bf16 v[66:69], v[164:167], v[196:199], v[66:69]
	v_mfma_f32_16x16x32_bf16 v[66:69], v[168:171], v[200:203], v[66:69]
	v_mfma_f32_16x16x32_bf16 v[78:81], v[168:171], v[192:195], v[78:81]
	v_mfma_f32_16x16x32_bf16 v[78:81], v[164:167], v[188:191], v[78:81]
	v_mfma_f32_16x16x32_bf16 v[94:97], v[164:167], v[180:183], v[94:97]
	v_mfma_f32_16x16x32_bf16 v[94:97], v[168:171], v[184:187], v[94:97]
	v_mfma_f32_16x16x32_bf16 v[110:113], v[168:171], v[176:179], v[110:113]
	v_mfma_f32_16x16x32_bf16 v[110:113], v[164:167], v[172:175], v[110:113]
	s_barrier
	s_mov_b32 m0, s24
	s_mov_b32 s10, s6
	s_mov_b32 s11, s7
	ds_read_b128 v[172:175], v139 offset:16384
	ds_read_b128 v[176:179], v139 offset:17408
	ds_read_b128 v[180:183], v139 offset:18432
	ds_read_b128 v[184:187], v139 offset:19456
	ds_read_b128 v[188:191], v139 offset:20480
	ds_read_b128 v[192:195], v139 offset:21504
	ds_read_b128 v[196:199], v139 offset:22528
	ds_read_b128 v[200:203], v139 offset:23552
	buffer_load_dwordx4 v135, s[8:11], s52 offen lds
	s_mov_b32 m0, s26
	s_add_i32 s54, s52, 0x200000
	buffer_load_dwordx4 v137, s[8:11], s52 offen lds
	s_mov_b32 m0, s27
	s_nop 0
	buffer_load_dwordx4 v135, s[8:11], s54 offen lds
	s_mov_b32 m0, s28
	s_nop 0
	buffer_load_dwordx4 v137, s[8:11], s54 offen lds
	s_mov_b32 m0, s23
	s_nop 0
	buffer_load_dwordx4 v134, s[4:7], s53 offen lds
	s_mov_b32 m0, s29
	s_nop 0
	buffer_load_dwordx4 v136, s[4:7], s53 offen lds
	s_waitcnt vmcnt(8)
	s_waitcnt lgkmcnt(0)
	s_barrier
	s_waitcnt lgkmcnt(7)
	v_mfma_f32_16x16x32_bf16 v[62:65], v[140:143], v[172:175], v[62:65]
	v_mfma_f32_16x16x32_bf16 v[62:65], v[144:147], v[176:179], v[62:65]
	s_waitcnt lgkmcnt(5)
	v_mfma_f32_16x16x32_bf16 v[50:53], v[144:147], v[184:187], v[50:53]
	v_mfma_f32_16x16x32_bf16 v[50:53], v[140:143], v[180:183], v[50:53]
	s_waitcnt lgkmcnt(3)
	v_mfma_f32_16x16x32_bf16 v[34:37], v[140:143], v[188:191], v[34:37]
	v_mfma_f32_16x16x32_bf16 v[34:37], v[144:147], v[192:195], v[34:37]
	s_waitcnt lgkmcnt(1)
	v_mfma_f32_16x16x32_bf16 v[18:21], v[144:147], v[200:203], v[18:21]
	v_mfma_f32_16x16x32_bf16 v[18:21], v[140:143], v[196:199], v[18:21]
	v_mfma_f32_16x16x32_bf16 v[10:13], v[148:151], v[196:199], v[10:13]
	v_mfma_f32_16x16x32_bf16 v[10:13], v[152:155], v[200:203], v[10:13]
	v_mfma_f32_16x16x32_bf16 v[26:29], v[152:155], v[192:195], v[26:29]
	v_mfma_f32_16x16x32_bf16 v[26:29], v[148:151], v[188:191], v[26:29]
	v_mfma_f32_16x16x32_bf16 v[42:45], v[148:151], v[180:183], v[42:45]
	v_mfma_f32_16x16x32_bf16 v[42:45], v[152:155], v[184:187], v[42:45]
	s_waitcnt lgkmcnt(0)
	v_mfma_f32_16x16x32_bf16 v[58:61], v[152:155], v[176:179], v[58:61]
	v_mfma_f32_16x16x32_bf16 v[58:61], v[148:151], v[172:175], v[58:61]
	v_mfma_f32_16x16x32_bf16 v[54:57], v[156:159], v[172:175], v[54:57]
	v_mfma_f32_16x16x32_bf16 v[54:57], v[160:163], v[176:179], v[54:57]
	v_mfma_f32_16x16x32_bf16 v[38:41], v[160:163], v[184:187], v[38:41]
	v_mfma_f32_16x16x32_bf16 v[38:41], v[156:159], v[180:183], v[38:41]
	v_mfma_f32_16x16x32_bf16 v[22:25], v[156:159], v[188:191], v[22:25]
	v_mfma_f32_16x16x32_bf16 v[22:25], v[160:163], v[192:195], v[22:25]
	v_mfma_f32_16x16x32_bf16 v[6:9], v[160:163], v[200:203], v[6:9]
	v_mfma_f32_16x16x32_bf16 v[6:9], v[156:159], v[196:199], v[6:9]
	v_mfma_f32_16x16x32_bf16 v[2:5], v[164:167], v[196:199], v[2:5]
	v_mfma_f32_16x16x32_bf16 v[2:5], v[168:171], v[200:203], v[2:5]
	v_mfma_f32_16x16x32_bf16 v[14:17], v[168:171], v[192:195], v[14:17]
	v_mfma_f32_16x16x32_bf16 v[14:17], v[164:167], v[188:191], v[14:17]
	v_mfma_f32_16x16x32_bf16 v[30:33], v[164:167], v[180:183], v[30:33]
	v_mfma_f32_16x16x32_bf16 v[30:33], v[168:171], v[184:187], v[30:33]
	v_mfma_f32_16x16x32_bf16 v[46:49], v[168:171], v[176:179], v[46:49]
	v_mfma_f32_16x16x32_bf16 v[46:49], v[164:167], v[172:175], v[46:49]
	s_barrier
	v_add_u32_e32 v152, 0x18000, v138
	v_add_u32_e32 v168, 0x1c000, v138
	ds_read_b128 v[140:143], v152
	ds_read_b128 v[144:147], v152 offset:1024
	ds_read_b128 v[148:151], v152 offset:2048
	ds_read_b128 v[152:155], v152 offset:3072
	ds_read_b128 v[156:159], v168
	ds_read_b128 v[160:163], v168 offset:1024
	ds_read_b128 v[164:167], v168 offset:2048
	ds_read_b128 v[168:171], v168 offset:3072
	s_add_i32 s53, s53, 0x200000
	s_mov_b32 m0, s31
	ds_read_b128 v[172:175], v139 offset:32768
	ds_read_b128 v[176:179], v139 offset:33792
	ds_read_b128 v[180:183], v139 offset:34816
	ds_read_b128 v[184:187], v139 offset:35840
	ds_read_b128 v[188:191], v139 offset:36864
	ds_read_b128 v[192:195], v139 offset:37888
	ds_read_b128 v[196:199], v139 offset:38912
	ds_read_b128 v[200:203], v139 offset:39936
	buffer_load_dwordx4 v134, s[4:7], s53 offen lds
	s_mov_b32 m0, s33
	s_nop 0
	buffer_load_dwordx4 v136, s[4:7], s53 offen lds
	s_waitcnt vmcnt(8)
	s_waitcnt lgkmcnt(0)
	s_barrier
	s_waitcnt lgkmcnt(7)
	v_mfma_f32_16x16x32_bf16 v[126:129], v[140:143], v[172:175], v[126:129]
	v_mfma_f32_16x16x32_bf16 v[126:129], v[144:147], v[176:179], v[126:129]
	s_waitcnt lgkmcnt(5)
	v_mfma_f32_16x16x32_bf16 v[114:117], v[144:147], v[184:187], v[114:117]
	v_mfma_f32_16x16x32_bf16 v[114:117], v[140:143], v[180:183], v[114:117]
	s_waitcnt lgkmcnt(3)
	v_mfma_f32_16x16x32_bf16 v[98:101], v[140:143], v[188:191], v[98:101]
	v_mfma_f32_16x16x32_bf16 v[98:101], v[144:147], v[192:195], v[98:101]
	s_waitcnt lgkmcnt(1)
	v_mfma_f32_16x16x32_bf16 v[82:85], v[144:147], v[200:203], v[82:85]
	v_mfma_f32_16x16x32_bf16 v[82:85], v[140:143], v[196:199], v[82:85]
	v_mfma_f32_16x16x32_bf16 v[74:77], v[148:151], v[196:199], v[74:77]
	v_mfma_f32_16x16x32_bf16 v[74:77], v[152:155], v[200:203], v[74:77]
	v_mfma_f32_16x16x32_bf16 v[90:93], v[152:155], v[192:195], v[90:93]
	v_mfma_f32_16x16x32_bf16 v[90:93], v[148:151], v[188:191], v[90:93]
	v_mfma_f32_16x16x32_bf16 v[106:109], v[148:151], v[180:183], v[106:109]
	v_mfma_f32_16x16x32_bf16 v[106:109], v[152:155], v[184:187], v[106:109]
	s_waitcnt lgkmcnt(0)
	v_mfma_f32_16x16x32_bf16 v[122:125], v[152:155], v[176:179], v[122:125]
	v_mfma_f32_16x16x32_bf16 v[122:125], v[148:151], v[172:175], v[122:125]
	v_mfma_f32_16x16x32_bf16 v[118:121], v[156:159], v[172:175], v[118:121]
	v_mfma_f32_16x16x32_bf16 v[118:121], v[160:163], v[176:179], v[118:121]
	v_mfma_f32_16x16x32_bf16 v[102:105], v[160:163], v[184:187], v[102:105]
	v_mfma_f32_16x16x32_bf16 v[102:105], v[156:159], v[180:183], v[102:105]
	v_mfma_f32_16x16x32_bf16 v[86:89], v[156:159], v[188:191], v[86:89]
	v_mfma_f32_16x16x32_bf16 v[86:89], v[160:163], v[192:195], v[86:89]
	v_mfma_f32_16x16x32_bf16 v[70:73], v[160:163], v[200:203], v[70:73]
	v_mfma_f32_16x16x32_bf16 v[70:73], v[156:159], v[196:199], v[70:73]
	v_mfma_f32_16x16x32_bf16 v[66:69], v[164:167], v[196:199], v[66:69]
	v_mfma_f32_16x16x32_bf16 v[66:69], v[168:171], v[200:203], v[66:69]
	v_mfma_f32_16x16x32_bf16 v[78:81], v[168:171], v[192:195], v[78:81]
	v_mfma_f32_16x16x32_bf16 v[78:81], v[164:167], v[188:191], v[78:81]
	v_mfma_f32_16x16x32_bf16 v[94:97], v[164:167], v[180:183], v[94:97]
	v_mfma_f32_16x16x32_bf16 v[94:97], v[168:171], v[184:187], v[94:97]
	v_mfma_f32_16x16x32_bf16 v[110:113], v[168:171], v[176:179], v[110:113]
	v_mfma_f32_16x16x32_bf16 v[110:113], v[164:167], v[172:175], v[110:113]
	s_barrier
	s_mov_b32 m0, s34
	s_or_b32 s53, s52, 0x80
	ds_read_b128 v[172:175], v139 offset:49152
	ds_read_b128 v[176:179], v139 offset:50176
	ds_read_b128 v[180:183], v139 offset:51200
	ds_read_b128 v[184:187], v139 offset:52224
	ds_read_b128 v[188:191], v139 offset:53248
	ds_read_b128 v[192:195], v139 offset:54272
	ds_read_b128 v[196:199], v139 offset:55296
	ds_read_b128 v[200:203], v139 offset:56320
	buffer_load_dwordx4 v135, s[8:11], s53 offen lds
	s_mov_b32 m0, s35
	s_add_i32 s52, s52, 0x200080
	buffer_load_dwordx4 v137, s[8:11], s53 offen lds
	s_mov_b32 m0, s39
	s_nop 0
	buffer_load_dwordx4 v135, s[8:11], s52 offen lds
	s_mov_b32 m0, s40
	s_nop 0
	buffer_load_dwordx4 v137, s[8:11], s52 offen lds
	s_mov_b32 m0, s37
	s_nop 0
	buffer_load_dwordx4 v134, s[4:7], s51 offen lds
	s_mov_b32 m0, s38
	s_nop 0
	buffer_load_dwordx4 v136, s[4:7], s51 offen lds
	s_waitcnt vmcnt(8)
	s_waitcnt lgkmcnt(0)
	s_barrier
	s_waitcnt lgkmcnt(7)
	v_mfma_f32_16x16x32_bf16 v[62:65], v[140:143], v[172:175], v[62:65]
	v_mfma_f32_16x16x32_bf16 v[62:65], v[144:147], v[176:179], v[62:65]
	s_waitcnt lgkmcnt(5)
	v_mfma_f32_16x16x32_bf16 v[50:53], v[144:147], v[184:187], v[50:53]
	v_mfma_f32_16x16x32_bf16 v[50:53], v[140:143], v[180:183], v[50:53]
	s_waitcnt lgkmcnt(3)
	v_mfma_f32_16x16x32_bf16 v[34:37], v[140:143], v[188:191], v[34:37]
	v_mfma_f32_16x16x32_bf16 v[34:37], v[144:147], v[192:195], v[34:37]
	s_waitcnt lgkmcnt(1)
	v_mfma_f32_16x16x32_bf16 v[18:21], v[144:147], v[200:203], v[18:21]
	v_mfma_f32_16x16x32_bf16 v[18:21], v[140:143], v[196:199], v[18:21]
	v_mfma_f32_16x16x32_bf16 v[10:13], v[148:151], v[196:199], v[10:13]
	v_mfma_f32_16x16x32_bf16 v[10:13], v[152:155], v[200:203], v[10:13]
	v_mfma_f32_16x16x32_bf16 v[26:29], v[152:155], v[192:195], v[26:29]
	v_mfma_f32_16x16x32_bf16 v[26:29], v[148:151], v[188:191], v[26:29]
	v_mfma_f32_16x16x32_bf16 v[42:45], v[148:151], v[180:183], v[42:45]
	v_mfma_f32_16x16x32_bf16 v[42:45], v[152:155], v[184:187], v[42:45]
	s_waitcnt lgkmcnt(0)
	v_mfma_f32_16x16x32_bf16 v[58:61], v[152:155], v[176:179], v[58:61]
	v_mfma_f32_16x16x32_bf16 v[58:61], v[148:151], v[172:175], v[58:61]
	v_mfma_f32_16x16x32_bf16 v[54:57], v[156:159], v[172:175], v[54:57]
	v_mfma_f32_16x16x32_bf16 v[54:57], v[160:163], v[176:179], v[54:57]
	v_mfma_f32_16x16x32_bf16 v[38:41], v[160:163], v[184:187], v[38:41]
	v_mfma_f32_16x16x32_bf16 v[38:41], v[156:159], v[180:183], v[38:41]
	v_mfma_f32_16x16x32_bf16 v[22:25], v[156:159], v[188:191], v[22:25]
	v_mfma_f32_16x16x32_bf16 v[22:25], v[160:163], v[192:195], v[22:25]
	v_mfma_f32_16x16x32_bf16 v[6:9], v[160:163], v[200:203], v[6:9]
	v_mfma_f32_16x16x32_bf16 v[6:9], v[156:159], v[196:199], v[6:9]
	v_mfma_f32_16x16x32_bf16 v[2:5], v[164:167], v[196:199], v[2:5]
	v_mfma_f32_16x16x32_bf16 v[2:5], v[168:171], v[200:203], v[2:5]
	v_mfma_f32_16x16x32_bf16 v[14:17], v[168:171], v[192:195], v[14:17]
	v_mfma_f32_16x16x32_bf16 v[14:17], v[164:167], v[188:191], v[14:17]
	v_mfma_f32_16x16x32_bf16 v[30:33], v[164:167], v[180:183], v[30:33]
	v_mfma_f32_16x16x32_bf16 v[30:33], v[168:171], v[184:187], v[30:33]
	v_mfma_f32_16x16x32_bf16 v[46:49], v[168:171], v[176:179], v[46:49]
	v_mfma_f32_16x16x32_bf16 v[46:49], v[164:167], v[172:175], v[46:49]
	s_barrier
	s_add_i32 s49, s49, 2
	s_addk_i32 s50, 0x100
	s_cmpk_gt_u32 s49, 0x7d
	s_cbranch_scc0 .LBB0_1029
	s_andn2_b64 vcc, exec, s[2:3]
	s_cbranch_vccnz .LBB0_1021
	v_mov_b32_e32 v2, 0
	s_mov_b32 s17, s44
	s_mov_b32 s14, s45
	s_mov_b32 s25, s46
	s_mov_b32 s30, s13
	s_mov_b32 s43, s12
	v_mov_b32_e32 v3, v2
	v_mov_b32_e32 v4, v2
	v_mov_b32_e32 v5, v2
	v_mov_b32_e32 v6, v2
	v_mov_b32_e32 v7, v2
	v_mov_b32_e32 v8, v2
	v_mov_b32_e32 v9, v2
	v_mov_b32_e32 v14, v2
	v_mov_b32_e32 v15, v2
	v_mov_b32_e32 v16, v2
	v_mov_b32_e32 v17, v2
	v_mov_b32_e32 v22, v2
	v_mov_b32_e32 v23, v2
	v_mov_b32_e32 v24, v2
	v_mov_b32_e32 v25, v2
	v_mov_b32_e32 v30, v2
	v_mov_b32_e32 v31, v2
	v_mov_b32_e32 v32, v2
	v_mov_b32_e32 v33, v2
	v_mov_b32_e32 v38, v2
	v_mov_b32_e32 v39, v2
	v_mov_b32_e32 v40, v2
	v_mov_b32_e32 v41, v2
	v_mov_b32_e32 v46, v2
	v_mov_b32_e32 v47, v2
	v_mov_b32_e32 v48, v2
	v_mov_b32_e32 v49, v2
	v_mov_b32_e32 v54, v2
	v_mov_b32_e32 v55, v2
	v_mov_b32_e32 v56, v2
	v_mov_b32_e32 v57, v2
	v_mov_b32_e32 v10, v2
	v_mov_b32_e32 v11, v2
	v_mov_b32_e32 v12, v2
	v_mov_b32_e32 v13, v2
	v_mov_b32_e32 v18, v2
	v_mov_b32_e32 v19, v2
	v_mov_b32_e32 v20, v2
	v_mov_b32_e32 v21, v2
	v_mov_b32_e32 v26, v2
	v_mov_b32_e32 v27, v2
	v_mov_b32_e32 v28, v2
	v_mov_b32_e32 v29, v2
	v_mov_b32_e32 v34, v2
	v_mov_b32_e32 v35, v2
	v_mov_b32_e32 v36, v2
	v_mov_b32_e32 v37, v2
	v_mov_b32_e32 v42, v2
	v_mov_b32_e32 v43, v2
	v_mov_b32_e32 v44, v2
	v_mov_b32_e32 v45, v2
	v_mov_b32_e32 v50, v2
	v_mov_b32_e32 v51, v2
	v_mov_b32_e32 v52, v2
	v_mov_b32_e32 v53, v2
	v_mov_b32_e32 v58, v2
	v_mov_b32_e32 v59, v2
	v_mov_b32_e32 v60, v2
	v_mov_b32_e32 v61, v2
	v_mov_b32_e32 v62, v2
	v_mov_b32_e32 v63, v2
	v_mov_b32_e32 v64, v2
	v_mov_b32_e32 v65, v2
	v_mov_b32_e32 v66, v2
	v_mov_b32_e32 v67, v2
	v_mov_b32_e32 v68, v2
	v_mov_b32_e32 v69, v2
	v_mov_b32_e32 v70, v2
	v_mov_b32_e32 v71, v2
	v_mov_b32_e32 v72, v2
	v_mov_b32_e32 v73, v2
	v_mov_b32_e32 v78, v2
	v_mov_b32_e32 v79, v2
	v_mov_b32_e32 v80, v2
	v_mov_b32_e32 v81, v2
	v_mov_b32_e32 v86, v2
	v_mov_b32_e32 v87, v2
	v_mov_b32_e32 v88, v2
	v_mov_b32_e32 v89, v2
	v_mov_b32_e32 v94, v2
	v_mov_b32_e32 v95, v2
	v_mov_b32_e32 v96, v2
	v_mov_b32_e32 v97, v2
	v_mov_b32_e32 v102, v2
	v_mov_b32_e32 v103, v2
	v_mov_b32_e32 v104, v2
	v_mov_b32_e32 v105, v2
	v_mov_b32_e32 v110, v2
	v_mov_b32_e32 v111, v2
	v_mov_b32_e32 v112, v2
	v_mov_b32_e32 v113, v2
	v_mov_b32_e32 v118, v2
	v_mov_b32_e32 v119, v2
	v_mov_b32_e32 v120, v2
	v_mov_b32_e32 v121, v2
	v_mov_b32_e32 v74, v2
	v_mov_b32_e32 v75, v2
	v_mov_b32_e32 v76, v2
	v_mov_b32_e32 v77, v2
	v_mov_b32_e32 v82, v2
	v_mov_b32_e32 v83, v2
	v_mov_b32_e32 v84, v2
	v_mov_b32_e32 v85, v2
	v_mov_b32_e32 v90, v2
	v_mov_b32_e32 v91, v2
	v_mov_b32_e32 v92, v2
	v_mov_b32_e32 v93, v2
	v_mov_b32_e32 v98, v2
	v_mov_b32_e32 v99, v2
	v_mov_b32_e32 v100, v2
	v_mov_b32_e32 v101, v2
	v_mov_b32_e32 v106, v2
	v_mov_b32_e32 v107, v2
	v_mov_b32_e32 v108, v2
	v_mov_b32_e32 v109, v2
	v_mov_b32_e32 v114, v2
	v_mov_b32_e32 v115, v2
	v_mov_b32_e32 v116, v2
	v_mov_b32_e32 v117, v2
	v_mov_b32_e32 v122, v2
	v_mov_b32_e32 v123, v2
	v_mov_b32_e32 v124, v2
	v_mov_b32_e32 v125, v2
	v_mov_b32_e32 v126, v2
	v_mov_b32_e32 v127, v2
	v_mov_b32_e32 v128, v2
	v_mov_b32_e32 v129, v2
	s_branch .LBB0_1021
